# v037 + PV section: 3 more V-fragment LDS reads kept in flight (dead softmax regs)
# baseline (speedup 1.0000x reference)
.LBB3_141:
	s_mul_i32 s2, s41, 0x6000
	v_or_b32_e32 v98, s2, v206
	v_add_u32_e32 v250, 0x12000, v98
	ds_read_b128 v[98:101], v250 offset:8192
	v_cvt_pk_bf16_f32 v50, v50, v51
	v_cvt_pk_bf16_f32 v51, v52, v53
	v_cvt_pk_bf16_f32 v52, v54, v55
	v_cvt_pk_bf16_f32 v53, v56, v57
	ds_read_b128 v[54:57], v250 offset:9216
	v_cvt_pk_bf16_f32 v214, v82, v83
	v_cvt_pk_bf16_f32 v215, v84, v85
	ds_read_b128 v[82:85], v250 offset:13312
	s_waitcnt lgkmcnt(2)
	v_mfma_f32_32x32x16_bf16 v[114:129], v[98:101], v[50:53], 0
	ds_read_b128 v[98:101], v250 offset:12288
	v_cvt_pk_bf16_f32 v18, v18, v19
	v_cvt_pk_bf16_f32 v19, v20, v21
	v_cvt_pk_bf16_f32 v20, v22, v23
	v_cvt_pk_bf16_f32 v21, v24, v25
	v_cvt_pk_bf16_f32 v216, v86, v87
	v_cvt_pk_bf16_f32 v217, v88, v89
	v_cvt_pk_bf16_f32 v86, v10, v11
	s_waitcnt lgkmcnt(0)
	v_mfma_f32_32x32x16_bf16 v[98:113], v[98:101], v[50:53], 0
	v_cvt_pk_bf16_f32 v50, v58, v59
	v_cvt_pk_bf16_f32 v51, v60, v61
	v_cvt_pk_bf16_f32 v52, v62, v63
	v_cvt_pk_bf16_f32 v53, v64, v65
	ds_read_b128 v[58:61], v250 offset:10240
	v_cvt_pk_bf16_f32 v87, v12, v13
	v_cvt_pk_bf16_f32 v88, v14, v15
	v_mfma_f32_32x32x16_bf16 v[114:129], v[54:57], v[50:53], v[114:129]
	v_cvt_pk_bf16_f32 v2, v2, v3
	v_cvt_pk_bf16_f32 v3, v4, v5
	v_cvt_pk_bf16_f32 v4, v6, v7
	v_cvt_pk_bf16_f32 v5, v8, v9
	v_cvt_pk_bf16_f32 v6, v42, v43
	v_cvt_pk_bf16_f32 v7, v44, v45
	v_cvt_pk_bf16_f32 v8, v46, v47
	v_mfma_f32_32x32x16_bf16 v[98:113], v[82:85], v[50:53], v[98:113]
	ds_read_b128 v[22:25], v250 offset:14336
	ds_read_b128 v[50:53], v250 offset:11264
	ds_read_b128 v[10:13], v250
	v_cvt_pk_bf16_f32 v9, v48, v49
	v_cvt_pk_bf16_f32 v54, v90, v91
	v_cvt_pk_bf16_f32 v55, v92, v93
	v_cvt_pk_bf16_f32 v56, v94, v95
	v_cvt_pk_bf16_f32 v57, v96, v97
	s_waitcnt lgkmcnt(3)
	v_mfma_f32_32x32x16_bf16 v[114:129], v[58:61], v[18:21], v[114:129]
	v_cvt_pk_bf16_f32 v58, v34, v35
	v_cvt_pk_bf16_f32 v59, v36, v37
	ds_read_b128 v[34:37], v250 offset:15360
	v_cvt_pk_bf16_f32 v60, v38, v39
	v_cvt_pk_bf16_f32 v61, v40, v41
	v_cvt_pk_bf16_f32 v202, v66, v67
	v_cvt_pk_bf16_f32 v203, v68, v69
	s_waitcnt lgkmcnt(3)
	v_mfma_f32_32x32x16_bf16 v[98:113], v[22:25], v[18:21], v[98:113]
	v_cvt_pk_bf16_f32 v18, v26, v27
	v_cvt_pk_bf16_f32 v19, v28, v29
	v_cvt_pk_bf16_f32 v20, v30, v31
	v_cvt_pk_bf16_f32 v21, v32, v33
	v_cvt_pk_bf16_f32 v204, v70, v71
	v_cvt_pk_bf16_f32 v205, v72, v73
	v_cvt_pk_bf16_f32 v82, v74, v75
	s_waitcnt lgkmcnt(2)
	v_mfma_f32_32x32x16_bf16 v[114:129], v[50:53], v[18:21], v[114:129]
	v_cvt_pk_bf16_f32 v83, v76, v77
	v_cvt_pk_bf16_f32 v84, v78, v79
	v_cvt_pk_bf16_f32 v85, v80, v81
	s_lshl_b32 s2, s20, 6
	s_mov_b32 s41, 1
	s_mov_b64 s[20:21], 0
	s_nop 5
	v_max3_f32 v14, v114, s38, v115
	s_waitcnt lgkmcnt(0)
	v_mfma_f32_32x32x16_bf16 v[98:113], v[34:37], v[18:21], v[98:113]
	ds_read_b128 v[50:53], v250 offset:1024
	ds_read_b128 v[18:21], v250 offset:4096
	ds_read_b128 v[62:65], v250 offset:5120
	v_max3_f32 v14, v14, v116, v117
	v_max3_f32 v14, v14, v118, v119
	v_max3_f32 v14, v14, v120, v121
	v_max3_f32 v14, v14, v122, v123
	v_max3_f32 v14, v14, v124, v125
	v_max3_f32 v14, v14, v126, v127
	v_mfma_f32_32x32x16_bf16 v[34:49], v[214:217], v[10:13], 0
	v_max3_f32 v14, v14, v128, v129
	s_nop 0
	v_max3_f32 v14, v14, v98, v99
	v_max3_f32 v14, v14, v100, v101
	v_max3_f32 v14, v14, v102, v103
	v_max3_f32 v14, v14, v104, v105
	v_max3_f32 v14, v14, v106, v107
	v_max3_f32 v14, v14, v108, v109
	s_waitcnt lgkmcnt(1)
	v_mfma_f32_32x32x16_bf16 v[18:33], v[214:217], v[18:21], 0
	v_max3_f32 v14, v14, v110, v111
	v_max3_f32 v14, v14, v112, v113
	v_mov_b32_e32 v15, v14
	ds_read_b128 v[10:13], v250 offset:2048
	ds_read_b128 v[66:69], v250 offset:3072
	ds_read_b128 v[70:73], v250 offset:6144
	ds_read_b128 v[74:77], v250 offset:7168
	v_permlane32_swap_b32_e32 v14, v15
	v_max_f32_e32 v15, v15, v15
	v_mfma_f32_32x32x16_bf16 v[34:49], v[54:57], v[50:53], v[34:49]
	v_max_f32_e32 v14, v14, v14
	v_max_f32_e32 v14, v14, v15
	v_mul_f32_e32 v14, 0xbe38aa3b, v14
	v_fmamk_f32 v15, v114, 0x3e38aa3b, v14
	v_fmamk_f32 v50, v118, 0x3e38aa3b, v14
	v_exp_f32_e32 v50, v50
	v_fmamk_f32 v51, v119, 0x3e38aa3b, v14
	s_waitcnt lgkmcnt(4)
	v_mfma_f32_32x32x16_bf16 v[18:33], v[54:57], v[62:65], v[18:33]
	v_exp_f32_e32 v51, v51
	v_fmamk_f32 v52, v120, 0x3e38aa3b, v14
	v_exp_f32_e32 v52, v52
	v_fmamk_f32 v53, v121, 0x3e38aa3b, v14
	v_exp_f32_e32 v53, v53
	v_fmamk_f32 v109, v109, 0x3e38aa3b, v14
	s_waitcnt lgkmcnt(3)
	v_mfma_f32_32x32x16_bf16 v[34:49], v[58:61], v[10:13], v[34:49]
	v_exp_f32_e32 v10, v15
	v_fmamk_f32 v11, v115, 0x3e38aa3b, v14
	v_exp_f32_e32 v11, v11
	v_fmamk_f32 v12, v116, 0x3e38aa3b, v14
	v_exp_f32_e32 v12, v12
	v_fmamk_f32 v15, v117, 0x3e38aa3b, v14
	v_exp_f32_e32 v15, v15
	s_waitcnt lgkmcnt(1)
	v_mfma_f32_32x32x16_bf16 v[18:33], v[58:61], v[70:73], v[18:33]
	v_add_f32_e32 v13, 0, v10
	v_add_f32_e32 v13, v13, v11
	v_add_f32_e32 v13, v13, v12
	v_add_f32_e32 v13, v13, v15
	v_add_f32_e32 v13, v13, v50
	v_add_f32_e32 v13, v13, v51
	v_cvt_pk_bf16_f32 v10, v10, v11
	v_mfma_f32_32x32x16_bf16 v[34:49], v[6:9], v[66:69], v[34:49]
	v_cvt_pk_bf16_f32 v11, v12, v15
	v_cvt_pk_bf16_f32 v12, v50, v51
	s_waitcnt lgkmcnt(0)
	v_mfma_f32_32x32x16_bf16 v[18:33], v[6:9], v[74:77], v[18:33]
	v_fmamk_f32 v6, v122, 0x3e38aa3b, v14
	v_exp_f32_e32 v89, v6
	v_fmamk_f32 v6, v123, 0x3e38aa3b, v14
	v_exp_f32_e32 v94, v6
	v_fmamk_f32 v7, v124, 0x3e38aa3b, v14
	v_add_f32_e32 v6, v13, v52
	v_exp_f32_e32 v95, v7
	v_fmamk_f32 v7, v125, 0x3e38aa3b, v14
	v_add_f32_e32 v6, v6, v53
	v_exp_f32_e32 v96, v7
	v_fmamk_f32 v7, v126, 0x3e38aa3b, v14
	v_add_f32_e32 v6, v6, v89
	v_exp_f32_e32 v97, v7
	v_fmamk_f32 v7, v127, 0x3e38aa3b, v14
	v_add_f32_e32 v6, v6, v94
	v_exp_f32_e32 v114, v7
	v_fmamk_f32 v7, v128, 0x3e38aa3b, v14
	v_add_f32_e32 v6, v6, v95
	v_exp_f32_e32 v115, v7
	v_fmamk_f32 v7, v129, 0x3e38aa3b, v14
	v_add_f32_e32 v6, v6, v96
	v_exp_f32_e32 v116, v7
	v_fmamk_f32 v7, v98, 0x3e38aa3b, v14
	v_add_f32_e32 v6, v6, v97
	v_exp_f32_e32 v98, v7
	v_fmamk_f32 v7, v99, 0x3e38aa3b, v14
	v_add_f32_e32 v6, v6, v114
	v_exp_f32_e32 v99, v7
	v_fmamk_f32 v7, v100, 0x3e38aa3b, v14
	v_add_f32_e32 v6, v6, v115
	v_exp_f32_e32 v100, v7
	v_fmamk_f32 v7, v101, 0x3e38aa3b, v14
	v_add_f32_e32 v6, v6, v116
	v_exp_f32_e32 v101, v7
	v_fmamk_f32 v7, v102, 0x3e38aa3b, v14
	v_add_f32_e32 v6, v6, v98
	v_exp_f32_e32 v102, v7
	v_fmamk_f32 v7, v103, 0x3e38aa3b, v14
	v_add_f32_e32 v6, v6, v99
	v_exp_f32_e32 v103, v7
	v_add_f32_e32 v6, v6, v100
	v_add_f32_e32 v6, v6, v101
	v_add_f32_e32 v6, v6, v102
	v_add_f32_e32 v54, v6, v103
	v_fmamk_f32 v6, v104, 0x3e38aa3b, v14
	v_exp_f32_e32 v104, v6
	ds_read_b128 v[6:9], v250 offset:16384
	v_fmamk_f32 v13, v105, 0x3e38aa3b, v14
	v_exp_f32_e32 v105, v13
	v_cvt_pk_bf16_f32 v13, v52, v53
	ds_read_b128 v[50:53], v250 offset:18432
	ds_read_b128 v[90:93], v250 offset:17408
	ds_read_b128 v[118:121], v250 offset:19456
	ds_read_b128 v[122:125], v250 offset:20480
	ds_read_b128 v[126:129], v250 offset:22528
	s_waitcnt lgkmcnt(5)
	v_mfma_f32_32x32x16_bf16 v[66:81], v[6:9], v[10:13], 0
	v_add_f32_e32 v6, v54, v104
	v_add_f32_e32 v15, v6, v105
	v_fmamk_f32 v6, v106, 0x3e38aa3b, v14
	v_exp_f32_e32 v106, v6
	v_fmamk_f32 v6, v107, 0x3e38aa3b, v14
	v_exp_f32_e32 v107, v6
	s_waitcnt lgkmcnt(4)
	v_mfma_f32_32x32x16_bf16 v[50:65], v[50:53], v[10:13], 0
	v_fmamk_f32 v10, v108, 0x3e38aa3b, v14
	v_exp_f32_e32 v108, v10
	v_cvt_pk_bf16_f32 v10, v89, v94
	v_cvt_pk_bf16_f32 v11, v95, v96
	v_cvt_pk_bf16_f32 v12, v97, v114
	v_cvt_pk_bf16_f32 v13, v115, v116
	v_fmamk_f32 v94, v110, 0x3e38aa3b, v14
	v_exp_f32_e32 v89, v109
	s_waitcnt lgkmcnt(3)
	v_mfma_f32_32x32x16_bf16 v[66:81], v[90:93], v[10:13], v[66:81]
	v_exp_f32_e32 v109, v94
	v_add_f32_e32 v15, v15, v106
	v_add_f32_e32 v15, v15, v107
	v_add_f32_e32 v15, v15, v108
	v_add_f32_e32 v15, v15, v89
	v_add_f32_e32 v15, v15, v109
	s_waitcnt lgkmcnt(2)
	v_mfma_f32_32x32x16_bf16 v[50:65], v[118:121], v[10:13], v[50:65]
	v_cvt_pk_bf16_f32 v6, v98, v99
	v_cvt_pk_bf16_f32 v7, v100, v101
	v_cvt_pk_bf16_f32 v8, v102, v103
	v_cvt_pk_bf16_f32 v9, v104, v105
	ds_read_b128 v[94:97], v250 offset:21504
	s_waitcnt lgkmcnt(2)
	v_mfma_f32_32x32x16_bf16 v[66:81], v[122:125], v[6:9], v[66:81]
	v_fmamk_f32 v90, v111, 0x3e38aa3b, v14
	v_exp_f32_e32 v98, v90
	v_fmamk_f32 v90, v112, 0x3e38aa3b, v14
	v_fmac_f32_e32 v14, 0x3e38aa3b, v113
	v_exp_f32_e32 v99, v90
	ds_read_b128 v[90:93], v250 offset:23552
	v_add_f32_e32 v15, v15, v98
	s_waitcnt lgkmcnt(2)
	v_mfma_f32_32x32x16_bf16 v[50:65], v[126:129], v[6:9], v[50:65]
	v_exp_f32_e32 v11, v14
	v_add_f32_e32 v10, v15, v99
	v_cvt_pk_bf16_f32 v6, v106, v107
	v_cvt_pk_bf16_f32 v7, v108, v89
	v_cvt_pk_bf16_f32 v8, v109, v98
	v_cvt_pk_bf16_f32 v9, v99, v11
	v_add_f32_e32 v10, v10, v11
	v_mov_b32_e32 v11, v10
	s_waitcnt lgkmcnt(1)
	v_mfma_f32_32x32x16_bf16 v[66:81], v[94:97], v[6:9], v[66:81]
	v_permlane32_swap_b32_e32 v10, v11
	v_add_f32_e32 v10, v10, v11
	v_rcp_f32_e32 v101, v10
	v_cvt_pk_bf16_f32 v89, v16, v17
	v_ashrrev_i32_e32 v118, 3, v210
	v_and_b32_e32 v118, 0xffffffe0, v118
	v_bfe_u32 v119, v210, 6, 1
	v_add_u32_e32 v118, s16, v118
	v_lshl_or_b32 v118, v119, 4, v118
	v_or_b32_e32 v118, v118, v211
	v_lshlrev_b32_e32 v118, 10, v118
	v_add_u32_e32 v118, s2, v118
	v_bfe_u32 v119, v210, 7, 1
	v_lshl_or_b32 v118, v119, 5, v118
	v_or_b32_e32 v118, v118, v1
	v_lshlrev_b32_e32 v118, 2, v118
	global_load_dword v110, v118, s[12:13]
	global_load_dword v111, v118, s[72:73] offset:-4096
	global_load_dword v112, v118, s[72:73]
	global_load_dword v113, v118, s[76:77] offset:-4096
	global_load_dword v114, v118, s[76:77]
	global_load_dword v115, v118, s[78:79] offset:-4096
	global_load_dword v116, v118, s[78:79]
	global_load_dword v117, v118, s[74:75]
	s_nop 6
	s_waitcnt vmcnt(32)
	v_fmac_f32_e32 v245, v101, v70
	s_waitcnt lgkmcnt(0)
	v_mfma_f32_32x32x16_bf16 v[50:65], v[90:93], v[6:9], v[50:65]
	v_fmac_f32_e32 v243, v101, v71
	v_fmac_f32_e32 v241, v101, v72
	v_fmac_f32_e32 v239, v101, v73
	global_store_dword v252, v245, s[58:59] nt
	global_store_dword v252, v243, s[58:59] offset:1024 nt
	global_store_dword v252, v241, s[58:59] offset:2048 nt
	global_store_dword v252, v239, s[58:59] offset:3072 nt
	v_max3_f32 v6, v34, s38, v35
	v_max3_f32 v6, v6, v36, v37
	v_max3_f32 v6, v6, v38, v39
	v_max3_f32 v6, v6, v40, v41
	v_max3_f32 v7, v18, s38, v19
	v_max3_f32 v6, v6, v42, v43
	v_max3_f32 v7, v7, v20, v21
	v_max3_f32 v6, v6, v44, v45
	v_max3_f32 v7, v7, v22, v23
	v_max3_f32 v6, v6, v46, v47
	v_max3_f32 v7, v7, v24, v25
	v_max3_f32 v6, v6, v48, v49
	v_max3_f32 v7, v7, v26, v27
	v_max3_f32 v7, v7, v28, v29
	v_mov_b32_e32 v8, v6
	s_waitcnt vmcnt(32)
	v_fmac_f32_e32 v244, v101, v74
	v_fmac_f32_e32 v242, v101, v75
	v_fmac_f32_e32 v240, v101, v76
	v_fmac_f32_e32 v238, v101, v77
	global_store_dword v252, v244, s[60:61] nt
	global_store_dword v252, v242, s[60:61] offset:1024 nt
	global_store_dword v252, v240, s[60:61] offset:2048 nt
	global_store_dword v252, v238, s[60:61] offset:3072 nt
	v_max3_f32 v7, v7, v30, v31
	s_nop 0
	v_permlane32_swap_b32_e32 v6, v8
	v_max3_f32 v7, v7, v32, v33
	v_max_f32_e32 v8, v8, v8
	v_max_f32_e32 v6, v6, v6
	v_max_f32_e32 v90, v6, v8
	v_mov_b32_e32 v6, v7
	s_nop 1
	v_permlane32_swap_b32_e32 v7, v6
	v_mul_f32_e32 v8, 0xbe38aa3b, v90
	v_fmamk_f32 v9, v34, 0x3e38aa3b, v8
	v_max_f32_e32 v6, v6, v6
	v_max_f32_e32 v7, v7, v7
	v_exp_f32_e32 v9, v9
	s_waitcnt vmcnt(30)
	v_fmac_f32_e32 v236, v101, v78
	v_fmac_f32_e32 v234, v101, v79
	v_fmac_f32_e32 v232, v101, v80
	v_fmac_f32_e32 v230, v101, v81
	global_store_dword v252, v236, s[62:63] nt
	global_store_dword v252, v234, s[62:63] offset:1024 nt
	global_store_dword v252, v232, s[62:63] offset:2048 nt
	global_store_dword v252, v230, s[62:63] offset:3072 nt
	v_max_f32_e32 v91, v7, v6
	v_fmamk_f32 v7, v35, 0x3e38aa3b, v8
	v_exp_f32_e32 v7, v7
	v_fmamk_f32 v10, v36, 0x3e38aa3b, v8
	v_exp_f32_e32 v10, v10
	v_fmamk_f32 v11, v37, 0x3e38aa3b, v8
	v_exp_f32_e32 v11, v11
	v_fmamk_f32 v12, v38, 0x3e38aa3b, v8
	v_add_f32_e32 v6, 0, v9
	v_exp_f32_e32 v12, v12
	v_fmamk_f32 v13, v39, 0x3e38aa3b, v8
	v_add_f32_e32 v6, v6, v7
	v_exp_f32_e32 v13, v13
	v_fmamk_f32 v14, v40, 0x3e38aa3b, v8
	v_add_f32_e32 v6, v6, v10
	s_waitcnt vmcnt(32)
	v_fmac_f32_e32 v237, v101, v50
	v_fmac_f32_e32 v235, v101, v51
	v_fmac_f32_e32 v233, v101, v52
	v_fmac_f32_e32 v231, v101, v53
	global_store_dword v252, v237, s[64:65] nt
	global_store_dword v252, v235, s[64:65] offset:1024 nt
	global_store_dword v252, v233, s[64:65] offset:2048 nt
	global_store_dword v252, v231, s[64:65] offset:3072 nt
	v_exp_f32_e32 v14, v14
	v_fmamk_f32 v15, v41, 0x3e38aa3b, v8
	v_fmamk_f32 v16, v42, 0x3e38aa3b, v8
	v_add_f32_e32 v6, v6, v11
	v_exp_f32_e32 v15, v15
	v_exp_f32_e32 v92, v16
	v_fmamk_f32 v16, v43, 0x3e38aa3b, v8
	v_add_f32_e32 v6, v6, v12
	v_exp_f32_e32 v93, v16
	v_fmamk_f32 v16, v44, 0x3e38aa3b, v8
	v_add_f32_e32 v6, v6, v13
	v_exp_f32_e32 v94, v16
	v_fmamk_f32 v16, v45, 0x3e38aa3b, v8
	v_add_f32_e32 v6, v6, v14
	v_exp_f32_e32 v95, v16
	s_waitcnt vmcnt(32)
	v_fmac_f32_e32 v228, v101, v54
	v_fmac_f32_e32 v226, v101, v55
	v_fmac_f32_e32 v224, v101, v56
	v_fmac_f32_e32 v222, v101, v57
	global_store_dword v252, v228, s[66:67] nt
	global_store_dword v252, v226, s[66:67] offset:1024 nt
	global_store_dword v252, v224, s[66:67] offset:2048 nt
	global_store_dword v252, v222, s[66:67] offset:3072 nt
	v_fmamk_f32 v16, v46, 0x3e38aa3b, v8
	v_add_f32_e32 v6, v6, v15
	v_exp_f32_e32 v96, v16
	v_fmamk_f32 v16, v47, 0x3e38aa3b, v8
	v_add_f32_e32 v6, v6, v92
	v_exp_f32_e32 v97, v16
	v_fmamk_f32 v16, v48, 0x3e38aa3b, v8
	v_add_f32_e32 v6, v6, v93
	v_exp_f32_e32 v98, v16
	v_fmac_f32_e32 v8, 0x3e38aa3b, v49
	v_mul_f32_e32 v16, 0xbe38aa3b, v91
	v_add_f32_e32 v6, v6, v94
	v_exp_f32_e32 v99, v8
	v_fmamk_f32 v8, v18, 0x3e38aa3b, v16
	v_add_f32_e32 v6, v6, v95
	v_fmac_f32_e32 v249, v101, v66
	v_fmac_f32_e32 v248, v101, v67
	v_fmac_f32_e32 v247, v101, v68
	v_fmac_f32_e32 v246, v101, v69
	global_store_dword v252, v249, s[4:5] nt
	global_store_dword v252, v248, s[4:5] offset:1024 nt
	global_store_dword v252, v247, s[4:5] offset:2048 nt
	global_store_dword v252, v246, s[4:5] offset:3072 nt
	v_exp_f32_e32 v17, v8
	v_fmamk_f32 v8, v19, 0x3e38aa3b, v16
	v_add_f32_e32 v6, v6, v96
	v_exp_f32_e32 v18, v8
	v_fmamk_f32 v8, v20, 0x3e38aa3b, v16
	v_add_f32_e32 v6, v6, v97
	v_exp_f32_e32 v19, v8
	v_fmamk_f32 v8, v21, 0x3e38aa3b, v16
	v_add_f32_e32 v6, v6, v98
	v_exp_f32_e32 v20, v8
	v_fmamk_f32 v8, v22, 0x3e38aa3b, v16
	v_add_f32_e32 v100, v6, v99
	v_add_f32_e32 v6, 0, v17
	v_exp_f32_e32 v21, v8
	s_waitcnt vmcnt(32)
	v_fmac_f32_e32 v221, v101, v62
	v_fmac_f32_e32 v220, v101, v63
	v_fmac_f32_e32 v219, v101, v64
	v_fmac_f32_e32 v218, v101, v65
	global_store_dword v252, v221, s[70:71] nt
	global_store_dword v252, v220, s[70:71] offset:1024 nt
	global_store_dword v252, v219, s[70:71] offset:2048 nt
	global_store_dword v252, v218, s[70:71] offset:3072 nt
	v_fmamk_f32 v8, v23, 0x3e38aa3b, v16
	v_add_f32_e32 v6, v6, v18
	v_exp_f32_e32 v22, v8
	v_fmamk_f32 v8, v24, 0x3e38aa3b, v16
	v_add_f32_e32 v6, v6, v19
	v_exp_f32_e32 v23, v8
	v_fmamk_f32 v8, v25, 0x3e38aa3b, v16
	v_add_f32_e32 v6, v6, v20
	v_exp_f32_e32 v24, v8
	v_fmamk_f32 v8, v26, 0x3e38aa3b, v16
	v_add_f32_e32 v6, v6, v21
	v_exp_f32_e32 v25, v8
	v_add_f32_e32 v6, v6, v22
	v_add_f32_e32 v6, v6, v23
	v_fmac_f32_e32 v229, v101, v58
	v_fmac_f32_e32 v227, v101, v59
	v_fmac_f32_e32 v225, v101, v60
	v_fmac_f32_e32 v223, v101, v61
	global_store_dword v252, v229, s[68:69] nt
	global_store_dword v252, v227, s[68:69] offset:1024 nt
	global_store_dword v252, v225, s[68:69] offset:2048 nt
	global_store_dword v252, v223, s[68:69] offset:3072 nt
	v_add_f32_e32 v6, v6, v24
	v_add_f32_e32 v26, v6, v25
	v_fmamk_f32 v6, v27, 0x3e38aa3b, v16
	v_exp_f32_e32 v27, v6
	v_cvt_pk_bf16_f32 v6, v9, v7
	v_cvt_pk_bf16_f32 v7, v10, v11
	v_fmamk_f32 v10, v28, 0x3e38aa3b, v16
	v_cvt_pk_bf16_f32 v9, v14, v15
	v_exp_f32_e32 v28, v10
	v_fmamk_f32 v14, v29, 0x3e38aa3b, v16
	v_cvt_pk_bf16_f32 v8, v12, v13
	v_cvt_pk_bf16_f32 v13, v23, v24
	v_exp_f32_e32 v23, v14
	v_fmamk_f32 v14, v30, 0x3e38aa3b, v16
	v_mfma_f32_32x32x16_bf16 v[66:81], v[202:205], v[6:9], 0
	v_exp_f32_e32 v24, v14
	v_add_f32_e32 v14, v26, v27
	v_add_f32_e32 v14, v14, v28
	v_add_f32_e32 v14, v14, v23
	v_cvt_pk_bf16_f32 v10, v17, v18
	v_cvt_pk_bf16_f32 v11, v19, v20
	v_cvt_pk_bf16_f32 v12, v21, v22
	v_mfma_f32_32x32x16_bf16 v[34:49], v[2:5], v[6:9], 0
	v_fmamk_f32 v6, v31, 0x3e38aa3b, v16
	v_exp_f32_e32 v26, v6
	v_add_f32_e32 v14, v14, v24
	v_fmamk_f32 v6, v32, 0x3e38aa3b, v16
	v_fmac_f32_e32 v16, 0x3e38aa3b, v33
	v_exp_f32_e32 v29, v6
	v_exp_f32_e32 v30, v16
	v_mfma_f32_32x32x16_bf16 v[50:65], v[202:205], v[10:13], 0
	v_add_f32_e32 v18, v14, v26
	v_mov_b32_e32 v22, v100
	s_nop 1
	v_permlane32_swap_b32_e32 v100, v22
	v_add_f32_e32 v32, v100, v22
	v_cvt_pk_bf16_f32 v22, v25, v27
	v_cvt_pk_bf16_f32 v23, v28, v23
	v_mfma_f32_32x32x16_bf16 v[2:17], v[2:5], v[10:13], 0
	v_cvt_pk_bf16_f32 v24, v24, v26
	v_cvt_pk_bf16_f32 v25, v29, v30
	v_lshlrev_b32_e32 v26, 2, v213
	v_lshl_or_b32 v27, v212, 10, v26
	v_add_f32_e32 v18, v18, v29
	v_add_u32_e32 v28, 0x10000, v27
	v_add_f32_e32 v31, v18, v30
	v_mfma_f32_32x32x16_bf16 v[2:17], v[86:89], v[22:25], v[2:17]
	ds_write_b32 v28, v90
	v_add_u32_e32 v28, 0x10100, v27
	v_cvt_pk_bf16_f32 v18, v92, v93
	v_cvt_pk_bf16_f32 v19, v94, v95
	v_cvt_pk_bf16_f32 v20, v96, v97
	v_cvt_pk_bf16_f32 v21, v98, v99
	ds_write_b32 v28, v32
	v_mov_b32_e32 v28, v31
	v_mfma_f32_32x32x16_bf16 v[66:81], v[82:85], v[18:21], v[66:81]
	s_nop 0
	v_permlane32_swap_b32_e32 v31, v28
	s_nop 0
	v_cvt_pk_bf16_f32 v2, v2, v3
	v_cvt_pk_bf16_f32 v3, v4, v5
	v_cvt_pk_bf16_f32 v4, v6, v7
	v_cvt_pk_bf16_f32 v5, v8, v9
	v_mfma_f32_32x32x16_bf16 v[34:49], v[86:89], v[18:21], v[34:49]
	v_add_u32_e32 v19, 0x10200, v27
	v_add_f32_e32 v18, v31, v28
	ds_write_b32 v19, v91
	v_add_u32_e32 v19, 0x10300, v27
	ds_write_b32 v19, v18
	v_cvt_pk_bf16_f32 v18, v66, v67
	v_cvt_pk_bf16_f32 v19, v68, v69
	v_mfma_f32_32x32x16_bf16 v[50:65], v[82:85], v[22:25], v[50:65]
	v_lshl_or_b32 v22, v212, 13, v206
	ds_write_b128 v22, v[2:5] offset:6144
	v_cvt_pk_bf16_f32 v2, v10, v11
	v_cvt_pk_bf16_f32 v3, v12, v13
	v_cvt_pk_bf16_f32 v4, v14, v15
	v_cvt_pk_bf16_f32 v5, v16, v17
	ds_write_b128 v22, v[2:5] offset:7168
	v_bfe_u32 v16, v210, 6, 1
	v_ashrrev_i32_e32 v14, 7, v210
	v_and_b32_e32 v15, 1, v14
	v_cvt_pk_bf16_f32 v20, v70, v71
	v_cvt_pk_bf16_f32 v21, v72, v73
	ds_write_b128 v22, v[18:21]
	v_cvt_pk_bf16_f32 v18, v74, v75
	v_cvt_pk_bf16_f32 v19, v76, v77
	v_cvt_pk_bf16_f32 v20, v78, v79
	v_cvt_pk_bf16_f32 v21, v80, v81
	ds_write_b128 v22, v[18:21] offset:1024
	v_cvt_pk_bf16_f32 v18, v50, v51
	v_cvt_pk_bf16_f32 v19, v52, v53
	v_cvt_pk_bf16_f32 v20, v54, v55
	v_cvt_pk_bf16_f32 v21, v56, v57
	ds_write_b128 v22, v[18:21] offset:2048
	v_cvt_pk_bf16_f32 v18, v58, v59
	v_cvt_pk_bf16_f32 v19, v60, v61
	v_cvt_pk_bf16_f32 v20, v62, v63
	v_cvt_pk_bf16_f32 v21, v64, v65
	ds_write_b128 v22, v[18:21] offset:3072
	v_cvt_pk_bf16_f32 v18, v34, v35
	v_cvt_pk_bf16_f32 v19, v36, v37
	v_cvt_pk_bf16_f32 v20, v38, v39
	v_cvt_pk_bf16_f32 v21, v40, v41
	ds_write_b128 v22, v[18:21] offset:4096
	v_cvt_pk_bf16_f32 v18, v42, v43
	v_cvt_pk_bf16_f32 v19, v44, v45
	v_cvt_pk_bf16_f32 v20, v46, v47
	v_cvt_pk_bf16_f32 v21, v48, v49
	ds_write_b128 v22, v[18:21] offset:5120
	v_lshl_or_b32 v4, v15, 9, v26
	v_or_b32_e32 v5, 0x10000, v4
	v_or_b32_e32 v12, 0x10d00, v4
	s_waitcnt lgkmcnt(0)
	s_barrier
	v_or_b32_e32 v6, 0x10100, v4
	v_or_b32_e32 v7, 0x10400, v4
	v_or_b32_e32 v8, 0x10500, v4
	v_or_b32_e32 v9, 0x10800, v4
	v_or_b32_e32 v10, 0x10900, v4
	v_or_b32_e32 v11, 0x10c00, v4
	ds_read_b32 v5, v5
	ds_read_b32 v13, v6
	ds_read_b32 v15, v7
	ds_read_b32 v24, v8
	ds_read_b32 v25, v9
	ds_read_b32 v26, v10
	ds_read_b32 v27, v11
	ds_read_b32 v12, v12
	v_or_b32_e32 v6, 0x11000, v4
	v_or_b32_e32 v7, 0x11100, v4
	v_or_b32_e32 v8, 0x11400, v4
	v_or_b32_e32 v9, 0x11500, v4
	v_or_b32_e32 v10, 0x11800, v4
	v_or_b32_e32 v11, 0x11900, v4
	v_or_b32_e32 v28, 0x11c00, v4
	v_or_b32_e32 v4, 0x11d00, v4
	ds_read_b32 v29, v6
	ds_read_b32 v30, v7
	ds_read_b32 v31, v8
	ds_read_b32 v32, v9
	ds_read_b32 v33, v10
	ds_read_b32 v34, v11
	ds_read_b32 v28, v28
	ds_read_b32 v35, v4
	v_lshlrev_b32_e32 v44, 11, v14
	v_lshlrev_b32_e32 v45, 10, v16
	v_or3_b32 v44, v206, v44, v45
	ds_read_b128 v[48:51], v44
	ds_read_b128 v[52:55], v44 offset:8192
	ds_read_b128 v[56:59], v44 offset:16384
	ds_read_b128 v[60:63], v44 offset:24576
	ds_read_b128 v[64:67], v44 offset:32768
	ds_read_b128 v[68:71], v44 offset:40960
	ds_read_b128 v[72:75], v44 offset:49152
	ds_read_b128 v[76:79], v44 offset:57344
	s_waitcnt lgkmcnt(8)
	v_max_f32_e32 v4, v15, v15
	v_max_f32_e32 v6, v5, v5
	v_max_f32_e32 v4, v6, v4
	v_max3_f32 v4, v4, v25, v27
	v_max3_f32 v4, v4, v29, v31
	v_max3_f32 v36, v4, v33, v28
	v_sub_f32_e32 v4, v5, v36
	v_mul_f32_e32 v4, 0x3e38aa3b, v4
	v_exp_f32_e32 v37, v4
	s_nop 0
	v_fma_f32 v13, v13, v37, 0
	s_waitcnt lgkmcnt(7)
	v_lshlrev_b32_e32 v16, 16, v48
	v_and_b32_e32 v4, 0xffff0000, v48
	v_fma_f32 v38, v37, v4, 0
	v_lshlrev_b32_e32 v4, 16, v49
	v_fma_f32 v39, v37, v4, 0
	v_and_b32_e32 v4, 0xffff0000, v49
	v_sub_f32_e32 v5, v15, v36
	v_fma_f32 v40, v37, v4, 0
	v_lshlrev_b32_e32 v4, 16, v50
	v_mul_f32_e32 v5, 0x3e38aa3b, v5
	v_fma_f32 v41, v37, v4, 0
	v_and_b32_e32 v4, 0xffff0000, v50
	v_exp_f32_e32 v15, v5
	v_fma_f32 v42, v37, v4, 0
	v_lshlrev_b32_e32 v4, 16, v51
	v_fma_f32 v43, v37, v4, 0
	v_and_b32_e32 v4, 0xffff0000, v51
	v_fma_f32 v16, v37, v16, 0
	v_fma_f32 v37, v37, v4, 0
	s_waitcnt lgkmcnt(6)
	v_lshlrev_b32_e32 v4, 16, v52
	v_fmac_f32_e32 v16, v15, v4
	v_and_b32_e32 v4, 0xffff0000, v52
	v_fmac_f32_e32 v38, v15, v4
	v_lshlrev_b32_e32 v4, 16, v53
	v_fmac_f32_e32 v39, v15, v4
	v_and_b32_e32 v4, 0xffff0000, v53
	v_fmac_f32_e32 v40, v15, v4
	v_lshlrev_b32_e32 v4, 16, v54
	v_fmac_f32_e32 v41, v15, v4
	v_and_b32_e32 v4, 0xffff0000, v54
	v_fmac_f32_e32 v42, v15, v4
	v_lshlrev_b32_e32 v4, 16, v55
	v_fmac_f32_e32 v43, v15, v4
	v_sub_f32_e32 v4, v25, v36
	v_mul_f32_e32 v4, 0x3e38aa3b, v4
	v_fmac_f32_e32 v13, v24, v15
	v_exp_f32_e32 v24, v4
	v_and_b32_e32 v8, 0xffff0000, v55
	v_fmac_f32_e32 v37, v15, v8
	v_fmac_f32_e32 v13, v26, v24
	s_waitcnt lgkmcnt(5)
	v_lshlrev_b32_e32 v15, 16, v56
	v_and_b32_e32 v4, 0xffff0000, v56
	v_fmac_f32_e32 v38, v24, v4
	v_lshlrev_b32_e32 v4, 16, v57
	v_fmac_f32_e32 v39, v24, v4
	v_and_b32_e32 v4, 0xffff0000, v57
	v_sub_f32_e32 v5, v27, v36
	v_fmac_f32_e32 v40, v24, v4
	v_lshlrev_b32_e32 v4, 16, v58
	v_mul_f32_e32 v5, 0x3e38aa3b, v5
	v_fmac_f32_e32 v16, v24, v15
	v_fmac_f32_e32 v41, v24, v4
	v_and_b32_e32 v4, 0xffff0000, v58
	v_exp_f32_e32 v15, v5
	v_fmac_f32_e32 v42, v24, v4
	v_lshlrev_b32_e32 v4, 16, v59
	v_fmac_f32_e32 v43, v24, v4
	v_and_b32_e32 v4, 0xffff0000, v59
	v_fmac_f32_e32 v37, v24, v4
	s_waitcnt lgkmcnt(4)
	v_lshlrev_b32_e32 v4, 16, v60
	v_fmac_f32_e32 v16, v15, v4
	v_and_b32_e32 v4, 0xffff0000, v60
	v_fmac_f32_e32 v38, v15, v4
	v_lshlrev_b32_e32 v4, 16, v61
	v_fmac_f32_e32 v39, v15, v4
	v_and_b32_e32 v4, 0xffff0000, v61
	v_fmac_f32_e32 v40, v15, v4
	v_lshlrev_b32_e32 v4, 16, v62
	v_fmac_f32_e32 v41, v15, v4
	v_and_b32_e32 v4, 0xffff0000, v62
	v_fmac_f32_e32 v42, v15, v4
	v_lshlrev_b32_e32 v4, 16, v63
	v_fmac_f32_e32 v43, v15, v4
	v_sub_f32_e32 v4, v29, v36
	v_mul_f32_e32 v4, 0x3e38aa3b, v4
	v_fmac_f32_e32 v13, v12, v15
	v_exp_f32_e32 v12, v4
	v_and_b32_e32 v8, 0xffff0000, v63
	v_fmac_f32_e32 v37, v15, v8
	v_fmac_f32_e32 v13, v30, v12
	s_waitcnt lgkmcnt(3)
	v_lshlrev_b32_e32 v15, 16, v64
	v_and_b32_e32 v4, 0xffff0000, v64
	v_fmac_f32_e32 v38, v12, v4
	v_lshlrev_b32_e32 v4, 16, v65
	v_fmac_f32_e32 v39, v12, v4
	v_and_b32_e32 v4, 0xffff0000, v65
	v_sub_f32_e32 v5, v31, v36
	v_fmac_f32_e32 v40, v12, v4
	v_lshlrev_b32_e32 v4, 16, v66
	v_mul_f32_e32 v5, 0x3e38aa3b, v5
	v_fmac_f32_e32 v16, v12, v15
	v_fmac_f32_e32 v41, v12, v4
	v_and_b32_e32 v4, 0xffff0000, v66
	v_exp_f32_e32 v15, v5
	v_fmac_f32_e32 v42, v12, v4
	v_lshlrev_b32_e32 v4, 16, v67
	v_fmac_f32_e32 v43, v12, v4
	v_and_b32_e32 v4, 0xffff0000, v67
	v_fmac_f32_e32 v37, v12, v4
	s_waitcnt lgkmcnt(2)
	v_lshlrev_b32_e32 v4, 16, v68
	v_fmac_f32_e32 v16, v15, v4
	v_and_b32_e32 v4, 0xffff0000, v68
	v_fmac_f32_e32 v38, v15, v4
	v_lshlrev_b32_e32 v4, 16, v69
	v_fmac_f32_e32 v39, v15, v4
	v_and_b32_e32 v4, 0xffff0000, v69
	v_fmac_f32_e32 v40, v15, v4
	v_lshlrev_b32_e32 v4, 16, v70
	v_fmac_f32_e32 v41, v15, v4
	v_and_b32_e32 v4, 0xffff0000, v70
	v_fmac_f32_e32 v42, v15, v4
	v_lshlrev_b32_e32 v4, 16, v71
	v_fmac_f32_e32 v43, v15, v4
	v_sub_f32_e32 v4, v33, v36
	v_mul_f32_e32 v4, 0x3e38aa3b, v4
	v_exp_f32_e32 v12, v4
	v_and_b32_e32 v8, 0xffff0000, v71
	v_fmac_f32_e32 v37, v15, v8
	v_fmac_f32_e32 v13, v32, v15
	s_waitcnt lgkmcnt(1)
	v_lshlrev_b32_e32 v14, 16, v72
	v_and_b32_e32 v4, 0xffff0000, v72
	v_fmac_f32_e32 v38, v12, v4
	v_lshlrev_b32_e32 v4, 16, v73
	v_fmac_f32_e32 v39, v12, v4
	v_and_b32_e32 v4, 0xffff0000, v73
	v_sub_f32_e32 v5, v28, v36
	v_fmac_f32_e32 v40, v12, v4
	v_lshlrev_b32_e32 v4, 16, v74
	v_mul_f32_e32 v5, 0x3e38aa3b, v5
	v_fmac_f32_e32 v41, v12, v4
	v_and_b32_e32 v4, 0xffff0000, v74
	v_exp_f32_e32 v5, v5
	v_fmac_f32_e32 v42, v12, v4
	v_lshlrev_b32_e32 v4, 16, v75
	v_fmac_f32_e32 v43, v12, v4
	v_and_b32_e32 v4, 0xffff0000, v75
	v_fmac_f32_e32 v16, v12, v14
	v_fmac_f32_e32 v37, v12, v4
	s_waitcnt lgkmcnt(0)
	v_lshlrev_b32_e32 v4, 16, v76
	v_fmac_f32_e32 v16, v5, v4
	v_and_b32_e32 v4, 0xffff0000, v76
	v_fmac_f32_e32 v38, v5, v4
	v_lshlrev_b32_e32 v4, 16, v77
	v_fmac_f32_e32 v13, v34, v12
	v_fmac_f32_e32 v39, v5, v4
	v_and_b32_e32 v4, 0xffff0000, v77
	v_fmac_f32_e32 v13, v35, v5
	v_fmac_f32_e32 v40, v5, v4
	v_lshlrev_b32_e32 v4, 16, v78
	v_fmac_f32_e32 v41, v5, v4
	v_and_b32_e32 v4, 0xffff0000, v78
	v_rcp_f32_e32 v6, v13
	v_fmac_f32_e32 v42, v5, v4
	v_lshlrev_b32_e32 v4, 16, v79
	v_fmac_f32_e32 v43, v5, v4
	v_and_b32_e32 v4, 0xffff0000, v79
	v_fmac_f32_e32 v37, v5, v4
	s_waitcnt vmcnt(32)
	v_fmac_f32_e32 v111, v6, v38
	v_fmac_f32_e32 v112, v6, v39
	global_store_dword v118, v111, s[80:81] offset:-4096 nt
	global_store_dword v118, v112, s[80:81] nt
	v_fmac_f32_e32 v117, v6, v40
	global_store_dword v118, v117, s[82:83] nt
	v_fmac_f32_e32 v113, v6, v41
	global_store_dword v118, v113, s[84:85] offset:-4096 nt
	v_fmac_f32_e32 v114, v6, v42
	global_store_dword v118, v114, s[84:85] nt
	v_fmac_f32_e32 v110, v6, v16
	global_store_dword v118, v110, s[14:15] nt
	v_fmac_f32_e32 v115, v6, v43
	v_fmac_f32_e32 v116, v6, v37
	s_and_b64 vcc, exec, s[18:19]
	global_store_dword v118, v115, s[86:87] offset:-4096 nt
	global_store_dword v118, v116, s[86:87] nt
	s_barrier
	s_cbranch_vccnz .LBB3_144
